# first-arriving workgroup of each XCD issues an early L2 write-back at the barriers that follow GEMM phases (on top of interleaved wave index)
# baseline (speedup 1.0000x reference)
.LBB0_491:
	s_or_b64 exec, exec, s[2:3]
	v_cvt_f32_u32_e32 v5, v3
	s_waitcnt vmcnt(0)
	v_readfirstlane_b32 s2, v4
	v_sub_u32_e32 v4, 0, v3
	v_rcp_iflag_f32_e32 v5, v5
	v_add_u32_e32 v6, s2, v1
	v_mul_f32_e32 v5, 0x4f7ffffe, v5
	v_cvt_u32_f32_e32 v5, v5
	v_mul_lo_u32 v1, v4, v5
	v_mul_hi_u32 v1, v5, v1
	v_add_u32_e32 v1, v5, v1
	v_mul_hi_u32 v1, v6, v1
	v_mul_lo_u32 v4, v1, v3
	v_sub_u32_e32 v4, v6, v4
	v_add_u32_e32 v5, 1, v1
	v_cmp_ge_u32_e32 vcc, v4, v3
	s_nop 1
	v_cndmask_b32_e32 v1, v1, v5, vcc
	v_sub_u32_e32 v5, v4, v3
	v_cndmask_b32_e32 v4, v4, v5, vcc
	v_add_u32_e32 v5, 1, v1
	v_cmp_ge_u32_e32 vcc, v4, v3
	v_add_u32_e32 v4, 1, v6
	s_nop 0
	v_cndmask_b32_e32 v1, v1, v5, vcc
	v_mul_lo_u32 v5, v3, v1
	v_add_u32_e32 v3, v5, v3
	v_cmp_ne_u32_e32 vcc, v4, v3
	s_and_saveexec_b64 s[2:3], vcc
	s_xor_b64 s[2:3], exec, s[2:3]
	s_cbranch_execz .LBB0_505
	v_cmp_eq_u32_e32 vcc, v6, v5
	s_and_b64 vcc, exec, vcc
	s_cbranch_vccz .Lnofirst_0
	buffer_wbl2 sc1
.Lnofirst_0:
	v_readlane_b32 s4, v251, 16
	v_readlane_b32 s5, v251, 17
	s_waitcnt lgkmcnt(0)
	s_nop 3
	global_load_dword v2, v67, s[4:5] sc1
	s_waitcnt vmcnt(0)
	v_cmp_eq_u32_e32 vcc, v2, v1
	s_and_saveexec_b64 s[4:5], vcc
	s_cbranch_execz .LBB0_504
	s_mov_b32 s8, 1
	s_mov_b64 s[36:37], 0
	s_branch .LBB0_495

.Lnofirst_5:
	v_readlane_b32 s4, v251, 16
	v_readlane_b32 s5, v251, 17
	s_waitcnt lgkmcnt(0)
	s_nop 3
	global_load_dword v2, v67, s[4:5] sc1
	s_waitcnt vmcnt(0)
	v_cmp_eq_u32_e32 vcc, v2, v1
	s_and_saveexec_b64 s[4:5], vcc
	s_cbranch_execz .LBB0_1730
	s_mov_b32 s10, 1
	s_mov_b64 s[36:37], 0
	s_branch .LBB0_1721
